# v8 + 16 of 128 expert weight mats converted to fp8 by the idle att-half WGs during the ut_att phases instead of in the prologue (P=112,Q=120)
# speedup vs baseline: 1.0096x; 1.0075x over previous
.LBB0_654:
	s_barrier
	v_readlane_b32 s46, v255, 4
	s_sub_i32 s42, s88, 0x80
	s_lshl_b32 s42, s42, 3
	s_lshr_b32 s5, s33, 6
	s_add_i32 s42, s42, s5
	s_mul_i32 s5, s5, 0x4200
	s_movk_i32 s45, 120
	s_movk_i32 s4, 8
	s_movk_i32 vcc_lo, 112
	s_movk_i32 vcc_hi, 8
	s_cmp_eq_u32 s46, 1
	s_cselect_b32 s45, vcc_lo, s45
	s_cselect_b32 s4, vcc_hi, s4
	s_lshl_b32 s44, s4, 9
	s_mul_i32 s43, s4, 0x300
	v_readlane_b32 s8, v252, 0
	v_readlane_b32 s9, v252, 1
	v_mbcnt_lo_u32_b32 v13, -1, 0
	v_mbcnt_hi_u32_b32 v13, -1, v13
	s_load_dwordx2 s[6:7], s[8:9], 0xa0
	s_load_dwordx2 s[10:11], s[8:9], 0xd8
	s_load_dwordx2 s[8:9], s[8:9], 0xb0
	s_movk_i32 s46, 0x84
	s_movk_i32 s47, 0x840
	v_and_b32_e32 v14, 31, v13
	v_lshlrev_b32_e32 v14, 2, v14
	v_lshrrev_b32_e32 v15, 5, v13
	v_mov_b32_e32 v4, s5
	v_mad_u32_u24 v4, v15, s46, v4
	v_add_u32_e32 v4, v4, v14
	v_and_b32_e32 v10, 7, v13
	v_lshrrev_b32_e32 v11, 3, v13
	v_mov_b32_e32 v5, s5
	v_mad_u32_u24 v5, v10, s47, v5
	v_lshl_add_u32 v5, v11, 2, v5
	v_lshlrev_b32_e32 v6, 10, v11
	v_lshl_add_u32 v6, v10, 4, v6
	v_add_u32_e32 v7, 0x2000, v6
	v_add_u32_e32 v8, 0x4000, v6
	v_add_u32_e32 v9, 0x6000, v6
	s_waitcnt lgkmcnt(0)
	s_cmp_lt_u32 s42, s43
	s_cbranch_scc0 .Lcv_done
	s_cmp_lt_u32 s42, s44
	s_cbranch_scc0 .Lcv_dn0
	s_lshr_b32 s4, s42, 9
	s_add_i32 s4, s4, s45
	s_bfe_u32 s5, s42, 0x30006
	s_and_b32 vcc_lo, s42, 63
	s_lshl_b32 s46, s4, 23
	s_lshl_b32 s47, s5, 20
	s_add_u32 s46, s46, s47
	s_lshl_b32 s47, vcc_lo, 7
	s_add_u32 s46, s46, s47
	s_add_u32 s46, s46, s6
	s_addc_u32 s47, s7, 0
	s_lshl_b32 s52, s4, 21
	s_add_u32 s52, s52, 0x4400000
	s_lshl_b32 s53, s5, 7
	s_add_u32 s52, s52, s53
	s_bfe_u32 s53, vcc_lo, 0x30002
	s_lshl_b32 s53, s53, 18
	s_add_u32 s52, s52, s53
	s_lshr_b32 s53, vcc_lo, 5
	s_lshl_b32 s53, s53, 17
	s_add_u32 s52, s52, s53
	s_and_b32 s53, vcc_lo, 3
	s_lshl_b32 s53, s53, 15
	s_add_u32 s52, s52, s53
	s_add_u32 s52, s52, s10
	s_addc_u32 s53, s11, 0
	s_mov_b32 s51, 0x42000000
	s_movk_i32 s5, 0x2000
	s_movk_i32 s4, 0x4000
	s_branch .Lcv_ld0

c_jobs:
	.long	4
	.long	2840
	.long	1024
	.long	0
	.long	1024
	.long	0
	.long	1
	.long	2
	.quad	2908160
	.quad	2097152
	.quad	2097152
	.long	0
	.long	0
	.long	4
	.long	2840
	.long	1024
	.long	1536
	.long	512
	.long	1024
	.long	1
	.long	2
	.quad	2908160
	.quad	2097152
	.quad	2097152
	.long	0
	.long	0
	.long	4
	.long	2840
	.long	1024
	.long	2048
	.long	128
	.long	1536
	.long	1
	.long	2
	.quad	2908160
	.quad	2097152
	.quad	2097152
	.long	0
	.long	0
	.long	4
	.long	2840
	.long	1024
	.long	2176
	.long	128
	.long	1664
	.long	1
	.long	2
	.quad	2908160
	.quad	2097152
	.quad	2097152
	.long	0
	.long	0
	.long	4
	.long	2840
	.long	1024
	.long	2304
	.long	128
	.long	1792
	.long	1
	.long	2
	.quad	2908160
	.quad	2097152
	.quad	2097152
	.long	0
	.long	0
	.long	4
	.long	2840
	.long	1024
	.long	2560
	.long	128
	.long	1920
	.long	1
	.long	2
	.quad	2908160
	.quad	2097152
	.quad	2097152
	.long	0
	.long	0
	.long	4
	.long	2840
	.long	1024
	.long	1024
	.long	512
	.long	0
	.long	0
	.long	2
	.quad	2908160
	.quad	10485760
	.quad	786432
	.long	0
	.long	0
	.long	4
	.long	2840
	.long	1024
	.long	2432
	.long	128
	.long	512
	.long	0
	.long	2
	.quad	2908160
	.quad	10485760
	.quad	786432
	.long	0
	.long	0
	.long	4
	.long	2840
	.long	1024
	.long	2688
	.long	128
	.long	640
	.long	0
	.long	2
	.quad	2908160
	.quad	10485760
	.quad	786432
	.long	0
	.long	0
	.long	5
	.long	1024
	.long	1024
	.long	0
	.long	1024
	.long	0
	.long	0
	.long	2
	.quad	1048576
	.quad	13631488
	.quad	1048576
	.long	64
	.long	0
	.long	13
	.long	256
	.long	2048
	.long	0
	.long	256
	.long	0
	.long	0
	.long	4
	.quad	524288
	.quad	17825792
	.quad	524288
	.long	0
	.long	0
	.long	15
	.long	6144
	.long	1024
	.long	0
	.long	2048
	.long	0
	.long	0
	.long	2
	.quad	6291456
	.quad	22020096
	.quad	4194304
	.long	32
	.long	0
	.long	15
	.long	6144
	.long	1024
	.long	4096
	.long	2048
	.long	2048
	.long	0
	.long	2
	.quad	6291456
	.quad	22020096
	.quad	4194304
	.long	32
	.long	0
	.long	15
	.long	6144
	.long	1024
	.long	2048
	.long	2048
	.long	0
	.long	0
	.long	2
	.quad	6291456
	.quad	38797312
	.quad	2097152
	.long	32
	.long	0
	.long	16
	.long	1024
	.long	2048
	.long	0
	.long	1024
	.long	0
	.long	0
	.long	2
	.quad	2097152
	.quad	51380224
	.quad	2097152
	.long	128
	.long	0
	.long	20
	.long	2048
	.long	1024
	.long	0
	.long	2048
	.long	0
	.long	2
	.long	112
	.quad	2097152
	.quad	71303168
	.quad	2097152
	.long	32
	.long	0
	.long	22
	.long	1024
	.long	1024
	.long	0
	.long	1024
	.long	0
	.long	0
	.long	112
	.quad	1048576
	.quad	608174080
	.quad	1048576
	.long	64
	.long	0
	.long	24
	.long	1024
	.long	256
	.long	0
	.long	1024
	.long	0
	.long	0
	.long	4
	.quad	262144
	.quad	59768832
	.quad	262144
	.long	0
	.long	0
	.long	25
	.long	1024
	.long	1024
	.long	0
	.long	1024
	.long	0
	.long	0
	.long	4
	.quad	1048576
	.quad	61865984
	.quad	1048576
	.long	32
	.long	0
	.size	c_jobs, 1216

	.type	__hip_cuid_b50e1a6430de2f85,@object
